# DSA top-k: DPP row_ror adds replace the 4 ds_bpermute round trips per threshold probe; fast emit path (ballot straight from v_cmp into SGPR pairs, batched lane-0 writes) when no tie-breaking is needed
# speedup vs baseline: 1.0123x; 1.0123x over previous
.Lmy_emit_done:
	v_mov_b64_e32 v[10:11], v[6:7]
	v_add_u32_e32 v84, 8, v84
	v_mov_b64_e32 v[8:9], v[4:5]
	v_mov_b64_e32 v[78:79], v[70:71]
	s_andn2_b64 exec, exec, s[58:59]
	s_cbranch_execz .LBB0_1625

.LBB0_842:
	s_or_b64 exec, exec, s[68:69]
	s_xor_b64 s[74:75], s[2:3], -1
	s_mov_b64 s[72:73], -1
	s_mov_b64 s[2:3], s[62:63]
	s_nop 1
	v_add_u32_dpp v10, v10, v10 row_ror:8 row_mask:0xf bank_mask:0xf
	s_nop 1
	v_add_u32_dpp v10, v10, v10 row_ror:4 row_mask:0xf bank_mask:0xf
	s_nop 1
	v_add_u32_dpp v10, v10, v10 row_ror:2 row_mask:0xf bank_mask:0xf
	s_nop 1
	v_add_u32_dpp v249, v10, v10 row_ror:1 row_mask:0xf bank_mask:0xf
	v_mov_b64_e32 v[12:13], v[8:9]
	s_and_saveexec_b64 s[68:69], s[74:75]
	s_cbranch_execz .LBB0_848
	s_movk_i32 s2, 0x100
	v_mov_b32_e32 v10, v8
	v_cmp_gt_i32_e32 vcc, s2, v249
	v_mov_b64_e32 v[12:13], v[10:11]
	s_and_saveexec_b64 s[2:3], vcc
	s_xor_b64 s[2:3], exec, s[2:3]
	s_cbranch_execz .LBB0_845
	v_cvt_f32_i32_e32 v8, v249
	v_mul_f32_e32 v10, 0.5, v72
	v_cmp_gt_i32_e32 vcc, 0, v248
	v_sub_f32_e32 v79, 0x437f8000, v8
	v_mov_b32_e32 v8, v11
	v_cndmask_b32_e32 v72, v72, v10, vcc
	v_mov_b64_e32 v[12:13], v[8:9]

.LBB0_873:
	s_or_b64 exec, exec, s[64:65]
	s_and_b64 s[0:1], exec, s[42:43]
	s_or_b64 s[58:59], s[0:1], s[58:59]
	v_or_b32_e32 v10, v161, v85
	s_movk_i32 s0, 0x104
	v_mul_lo_u32 v10, v10, s0
	v_add_u32_e32 v10, 0, v10
	v_mov_b32_e32 v11, 0
	s_cmp_eq_u64 s[62:63], 0
	s_cbranch_scc0 .Lmy_emit_slow
	s_cmp_eq_u64 s[16:17], 0
	s_cbranch_scc1 .Lmy_emit_own
	v_cmp_ge_u32_e64 s[0:1], v247, v8
	v_cmp_ge_u32_e64 s[2:3], v246, v8
	v_cmp_ge_u32_e64 s[64:65], v210, v8
	v_cmp_ge_u32_e64 s[66:67], v245, v8
	s_and_saveexec_b64 s[42:43], s[14:15]
	v_lshrrev_b64 v[12:13], v46, s[0:1]
	ds_write_b16 v10, v12
	v_lshrrev_b64 v[12:13], v46, s[2:3]
	ds_write_b16 v10, v12 offset:2
	v_lshrrev_b64 v[12:13], v46, s[64:65]
	ds_write_b16 v10, v12 offset:4
	v_lshrrev_b64 v[12:13], v46, s[66:67]
	ds_write_b16 v10, v12 offset:6
	s_or_b64 exec, exec, s[42:43]
	v_cmp_ge_u32_e64 s[0:1], v239, v8
	v_cmp_ge_u32_e64 s[2:3], v244, v8
	v_cmp_ge_u32_e64 s[64:65], v237, v8
	v_cmp_ge_u32_e64 s[66:67], v243, v8
	s_and_saveexec_b64 s[42:43], s[14:15]
	v_lshrrev_b64 v[12:13], v46, s[0:1]
	ds_write_b16 v10, v12 offset:8
	v_lshrrev_b64 v[12:13], v46, s[2:3]
	ds_write_b16 v10, v12 offset:10
	v_lshrrev_b64 v[12:13], v46, s[64:65]
	ds_write_b16 v10, v12 offset:12
	v_lshrrev_b64 v[12:13], v46, s[66:67]
	ds_write_b16 v10, v12 offset:14
	s_or_b64 exec, exec, s[42:43]
	s_cmp_eq_u64 s[18:19], 0
	s_cbranch_scc1 .Lmy_emit_own
	v_cmp_ge_u32_e64 s[0:1], v235, v8
	v_cmp_ge_u32_e64 s[2:3], v242, v8
	v_cmp_ge_u32_e64 s[64:65], v212, v8
	v_cmp_ge_u32_e64 s[66:67], v241, v8
	s_and_saveexec_b64 s[42:43], s[14:15]
	v_lshrrev_b64 v[12:13], v46, s[0:1]
	ds_write_b16 v10, v12 offset:16
	v_lshrrev_b64 v[12:13], v46, s[2:3]
	ds_write_b16 v10, v12 offset:18
	v_lshrrev_b64 v[12:13], v46, s[64:65]
	ds_write_b16 v10, v12 offset:20
	v_lshrrev_b64 v[12:13], v46, s[66:67]
	ds_write_b16 v10, v12 offset:22
	s_or_b64 exec, exec, s[42:43]
	v_cmp_ge_u32_e64 s[0:1], v209, v8
	v_cmp_ge_u32_e64 s[2:3], v240, v8
	v_cmp_ge_u32_e64 s[64:65], v207, v8
	v_cmp_ge_u32_e64 s[66:67], v238, v8
	s_and_saveexec_b64 s[42:43], s[14:15]
	v_lshrrev_b64 v[12:13], v46, s[0:1]
	ds_write_b16 v10, v12 offset:24
	v_lshrrev_b64 v[12:13], v46, s[2:3]
	ds_write_b16 v10, v12 offset:26
	v_lshrrev_b64 v[12:13], v46, s[64:65]
	ds_write_b16 v10, v12 offset:28
	v_lshrrev_b64 v[12:13], v46, s[66:67]
	ds_write_b16 v10, v12 offset:30
	s_or_b64 exec, exec, s[42:43]
	s_cmp_eq_u64 s[20:21], 0
	s_cbranch_scc1 .Lmy_emit_own
	v_cmp_ge_u32_e64 s[0:1], v205, v8
	v_cmp_ge_u32_e64 s[2:3], v236, v8
	v_cmp_ge_u32_e64 s[64:65], v203, v8
	v_cmp_ge_u32_e64 s[66:67], v213, v8
	s_and_saveexec_b64 s[42:43], s[14:15]
	v_lshrrev_b64 v[12:13], v46, s[0:1]
	ds_write_b16 v10, v12 offset:32
	v_lshrrev_b64 v[12:13], v46, s[2:3]
	ds_write_b16 v10, v12 offset:34
	v_lshrrev_b64 v[12:13], v46, s[64:65]
	ds_write_b16 v10, v12 offset:36
	v_lshrrev_b64 v[12:13], v46, s[66:67]
	ds_write_b16 v10, v12 offset:38
	s_or_b64 exec, exec, s[42:43]
	v_cmp_ge_u32_e64 s[0:1], v201, v8
	v_cmp_ge_u32_e64 s[2:3], v211, v8
	v_cmp_ge_u32_e64 s[64:65], v199, v8
	v_cmp_ge_u32_e64 s[66:67], v208, v8
	s_and_saveexec_b64 s[42:43], s[14:15]
	v_lshrrev_b64 v[12:13], v46, s[0:1]
	ds_write_b16 v10, v12 offset:40
	v_lshrrev_b64 v[12:13], v46, s[2:3]
	ds_write_b16 v10, v12 offset:42
	v_lshrrev_b64 v[12:13], v46, s[64:65]
	ds_write_b16 v10, v12 offset:44
	v_lshrrev_b64 v[12:13], v46, s[66:67]
	ds_write_b16 v10, v12 offset:46
	s_or_b64 exec, exec, s[42:43]
	s_cmp_eq_u64 s[8:9], 0
	s_cbranch_scc1 .Lmy_emit_own
	v_cmp_ge_u32_e64 s[0:1], v197, v8
	v_cmp_ge_u32_e64 s[2:3], v206, v8
	v_cmp_ge_u32_e64 s[64:65], v195, v8
	v_cmp_ge_u32_e64 s[66:67], v204, v8
	s_and_saveexec_b64 s[42:43], s[14:15]
	v_lshrrev_b64 v[12:13], v46, s[0:1]
	ds_write_b16 v10, v12 offset:48
	v_lshrrev_b64 v[12:13], v46, s[2:3]
	ds_write_b16 v10, v12 offset:50
	v_lshrrev_b64 v[12:13], v46, s[64:65]
	ds_write_b16 v10, v12 offset:52
	v_lshrrev_b64 v[12:13], v46, s[66:67]
	ds_write_b16 v10, v12 offset:54
	s_or_b64 exec, exec, s[42:43]
	v_cmp_ge_u32_e64 s[0:1], v193, v8
	v_cmp_ge_u32_e64 s[2:3], v202, v8
	v_cmp_ge_u32_e64 s[64:65], v191, v8
	v_cmp_ge_u32_e64 s[66:67], v200, v8
	s_and_saveexec_b64 s[42:43], s[14:15]
	v_lshrrev_b64 v[12:13], v46, s[0:1]
	ds_write_b16 v10, v12 offset:56
	v_lshrrev_b64 v[12:13], v46, s[2:3]
	ds_write_b16 v10, v12 offset:58
	v_lshrrev_b64 v[12:13], v46, s[64:65]
	ds_write_b16 v10, v12 offset:60
	v_lshrrev_b64 v[12:13], v46, s[66:67]
	ds_write_b16 v10, v12 offset:62
	s_or_b64 exec, exec, s[42:43]
	s_cmp_eq_u64 s[22:23], 0
	s_cbranch_scc1 .Lmy_emit_own
	v_cmp_ge_u32_e64 s[0:1], v189, v8
	v_cmp_ge_u32_e64 s[2:3], v198, v8
	v_cmp_ge_u32_e64 s[64:65], v187, v8
	v_cmp_ge_u32_e64 s[66:67], v196, v8
	s_and_saveexec_b64 s[42:43], s[14:15]
	v_lshrrev_b64 v[12:13], v46, s[0:1]
	ds_write_b16 v10, v12 offset:64
	v_lshrrev_b64 v[12:13], v46, s[2:3]
	ds_write_b16 v10, v12 offset:66
	v_lshrrev_b64 v[12:13], v46, s[64:65]
	ds_write_b16 v10, v12 offset:68
	v_lshrrev_b64 v[12:13], v46, s[66:67]
	ds_write_b16 v10, v12 offset:70
	s_or_b64 exec, exec, s[42:43]
	v_cmp_ge_u32_e64 s[0:1], v185, v8
	v_cmp_ge_u32_e64 s[2:3], v194, v8
	v_cmp_ge_u32_e64 s[64:65], v183, v8
	v_cmp_ge_u32_e64 s[66:67], v192, v8
	s_and_saveexec_b64 s[42:43], s[14:15]
	v_lshrrev_b64 v[12:13], v46, s[0:1]
	ds_write_b16 v10, v12 offset:72
	v_lshrrev_b64 v[12:13], v46, s[2:3]
	ds_write_b16 v10, v12 offset:74
	v_lshrrev_b64 v[12:13], v46, s[64:65]
	ds_write_b16 v10, v12 offset:76
	v_lshrrev_b64 v[12:13], v46, s[66:67]
	ds_write_b16 v10, v12 offset:78
	s_or_b64 exec, exec, s[42:43]
	s_cmp_eq_u64 s[24:25], 0
	s_cbranch_scc1 .Lmy_emit_own
	v_cmp_ge_u32_e64 s[0:1], v181, v8
	v_cmp_ge_u32_e64 s[2:3], v190, v8
	v_cmp_ge_u32_e64 s[64:65], v179, v8
	v_cmp_ge_u32_e64 s[66:67], v188, v8
	s_and_saveexec_b64 s[42:43], s[14:15]
	v_lshrrev_b64 v[12:13], v46, s[0:1]
	ds_write_b16 v10, v12 offset:80
	v_lshrrev_b64 v[12:13], v46, s[2:3]
	ds_write_b16 v10, v12 offset:82
	v_lshrrev_b64 v[12:13], v46, s[64:65]
	ds_write_b16 v10, v12 offset:84
	v_lshrrev_b64 v[12:13], v46, s[66:67]
	ds_write_b16 v10, v12 offset:86
	s_or_b64 exec, exec, s[42:43]
	v_cmp_ge_u32_e64 s[0:1], v177, v8
	v_cmp_ge_u32_e64 s[2:3], v186, v8
	v_cmp_ge_u32_e64 s[64:65], v175, v8
	v_cmp_ge_u32_e64 s[66:67], v184, v8
	s_and_saveexec_b64 s[42:43], s[14:15]
	v_lshrrev_b64 v[12:13], v46, s[0:1]
	ds_write_b16 v10, v12 offset:88
	v_lshrrev_b64 v[12:13], v46, s[2:3]
	ds_write_b16 v10, v12 offset:90
	v_lshrrev_b64 v[12:13], v46, s[64:65]
	ds_write_b16 v10, v12 offset:92
	v_lshrrev_b64 v[12:13], v46, s[66:67]
	ds_write_b16 v10, v12 offset:94
	s_or_b64 exec, exec, s[42:43]
	s_cmp_eq_u64 s[26:27], 0
	s_cbranch_scc1 .Lmy_emit_own
	v_cmp_ge_u32_e64 s[0:1], v173, v8
	v_cmp_ge_u32_e64 s[2:3], v182, v8
	v_cmp_ge_u32_e64 s[64:65], v171, v8
	v_cmp_ge_u32_e64 s[66:67], v180, v8
	s_and_saveexec_b64 s[42:43], s[14:15]
	v_lshrrev_b64 v[12:13], v46, s[0:1]
	ds_write_b16 v10, v12 offset:96
	v_lshrrev_b64 v[12:13], v46, s[2:3]
	ds_write_b16 v10, v12 offset:98
	v_lshrrev_b64 v[12:13], v46, s[64:65]
	ds_write_b16 v10, v12 offset:100
	v_lshrrev_b64 v[12:13], v46, s[66:67]
	ds_write_b16 v10, v12 offset:102
	s_or_b64 exec, exec, s[42:43]
	v_cmp_ge_u32_e64 s[0:1], v169, v8
	v_cmp_ge_u32_e64 s[2:3], v178, v8
	v_cmp_ge_u32_e64 s[64:65], v167, v8
	v_cmp_ge_u32_e64 s[66:67], v176, v8
	s_and_saveexec_b64 s[42:43], s[14:15]
	v_lshrrev_b64 v[12:13], v46, s[0:1]
	ds_write_b16 v10, v12 offset:104
	v_lshrrev_b64 v[12:13], v46, s[2:3]
	ds_write_b16 v10, v12 offset:106
	v_lshrrev_b64 v[12:13], v46, s[64:65]
	ds_write_b16 v10, v12 offset:108
	v_lshrrev_b64 v[12:13], v46, s[66:67]
	ds_write_b16 v10, v12 offset:110
	s_or_b64 exec, exec, s[42:43]
	s_cmp_eq_u64 s[10:11], 0
	s_cbranch_scc1 .Lmy_emit_own
	v_cmp_ge_u32_e64 s[0:1], v164, v8
	v_cmp_ge_u32_e64 s[2:3], v174, v8
	v_cmp_ge_u32_e64 s[64:65], v162, v8
	v_cmp_ge_u32_e64 s[66:67], v172, v8
	s_and_saveexec_b64 s[42:43], s[14:15]
	v_lshrrev_b64 v[12:13], v46, s[0:1]
	ds_write_b16 v10, v12 offset:112
	v_lshrrev_b64 v[12:13], v46, s[2:3]
	ds_write_b16 v10, v12 offset:114
	v_lshrrev_b64 v[12:13], v46, s[64:65]
	ds_write_b16 v10, v12 offset:116
	v_lshrrev_b64 v[12:13], v46, s[66:67]
	ds_write_b16 v10, v12 offset:118
	s_or_b64 exec, exec, s[42:43]
	v_cmp_ge_u32_e64 s[0:1], v159, v8
	v_cmp_ge_u32_e64 s[2:3], v170, v8
	v_cmp_ge_u32_e64 s[64:65], v157, v8
	v_cmp_ge_u32_e64 s[66:67], v168, v8
	s_and_saveexec_b64 s[42:43], s[14:15]
	v_lshrrev_b64 v[12:13], v46, s[0:1]
	ds_write_b16 v10, v12 offset:120
	v_lshrrev_b64 v[12:13], v46, s[2:3]
	ds_write_b16 v10, v12 offset:122
	v_lshrrev_b64 v[12:13], v46, s[64:65]
	ds_write_b16 v10, v12 offset:124
	v_lshrrev_b64 v[12:13], v46, s[66:67]
	ds_write_b16 v10, v12 offset:126
	s_or_b64 exec, exec, s[42:43]
	s_cmp_eq_u64 s[28:29], 0
	s_cbranch_scc1 .Lmy_emit_own
	v_cmp_ge_u32_e64 s[0:1], v155, v8
	v_cmp_ge_u32_e64 s[2:3], v166, v8
	v_cmp_ge_u32_e64 s[64:65], v153, v8
	v_cmp_ge_u32_e64 s[66:67], v165, v8
	s_and_saveexec_b64 s[42:43], s[14:15]
	v_lshrrev_b64 v[12:13], v46, s[0:1]
	ds_write_b16 v10, v12 offset:128
	v_lshrrev_b64 v[12:13], v46, s[2:3]
	ds_write_b16 v10, v12 offset:130
	v_lshrrev_b64 v[12:13], v46, s[64:65]
	ds_write_b16 v10, v12 offset:132
	v_lshrrev_b64 v[12:13], v46, s[66:67]
	ds_write_b16 v10, v12 offset:134
	s_or_b64 exec, exec, s[42:43]
	v_cmp_ge_u32_e64 s[0:1], v151, v8
	v_cmp_ge_u32_e64 s[2:3], v163, v8
	v_cmp_ge_u32_e64 s[64:65], v149, v8
	v_cmp_ge_u32_e64 s[66:67], v160, v8
	s_and_saveexec_b64 s[42:43], s[14:15]
	v_lshrrev_b64 v[12:13], v46, s[0:1]
	ds_write_b16 v10, v12 offset:136
	v_lshrrev_b64 v[12:13], v46, s[2:3]
	ds_write_b16 v10, v12 offset:138
	v_lshrrev_b64 v[12:13], v46, s[64:65]
	ds_write_b16 v10, v12 offset:140
	v_lshrrev_b64 v[12:13], v46, s[66:67]
	ds_write_b16 v10, v12 offset:142
	s_or_b64 exec, exec, s[42:43]
	s_cmp_eq_u64 s[30:31], 0
	s_cbranch_scc1 .Lmy_emit_own
	v_cmp_ge_u32_e64 s[0:1], v147, v8
	v_cmp_ge_u32_e64 s[2:3], v158, v8
	v_cmp_ge_u32_e64 s[64:65], v145, v8
	v_cmp_ge_u32_e64 s[66:67], v156, v8
	s_and_saveexec_b64 s[42:43], s[14:15]
	v_lshrrev_b64 v[12:13], v46, s[0:1]
	ds_write_b16 v10, v12 offset:144
	v_lshrrev_b64 v[12:13], v46, s[2:3]
	ds_write_b16 v10, v12 offset:146
	v_lshrrev_b64 v[12:13], v46, s[64:65]
	ds_write_b16 v10, v12 offset:148
	v_lshrrev_b64 v[12:13], v46, s[66:67]
	ds_write_b16 v10, v12 offset:150
	s_or_b64 exec, exec, s[42:43]
	v_cmp_ge_u32_e64 s[0:1], v144, v8
	v_cmp_ge_u32_e64 s[2:3], v154, v8
	v_cmp_ge_u32_e64 s[64:65], v142, v8
	v_cmp_ge_u32_e64 s[66:67], v152, v8
	s_and_saveexec_b64 s[42:43], s[14:15]
	v_lshrrev_b64 v[12:13], v46, s[0:1]
	ds_write_b16 v10, v12 offset:152
	v_lshrrev_b64 v[12:13], v46, s[2:3]
	ds_write_b16 v10, v12 offset:154
	v_lshrrev_b64 v[12:13], v46, s[64:65]
	ds_write_b16 v10, v12 offset:156
	v_lshrrev_b64 v[12:13], v46, s[66:67]
	ds_write_b16 v10, v12 offset:158
	s_or_b64 exec, exec, s[42:43]
	s_cmp_eq_u64 s[34:35], 0
	s_cbranch_scc1 .Lmy_emit_own
	v_cmp_ge_u32_e64 s[0:1], v140, v8
	v_cmp_ge_u32_e64 s[2:3], v150, v8
	v_cmp_ge_u32_e64 s[64:65], v138, v8
	v_cmp_ge_u32_e64 s[66:67], v148, v8
	s_and_saveexec_b64 s[42:43], s[14:15]
	v_lshrrev_b64 v[12:13], v46, s[0:1]
	ds_write_b16 v10, v12 offset:160
	v_lshrrev_b64 v[12:13], v46, s[2:3]
	ds_write_b16 v10, v12 offset:162
	v_lshrrev_b64 v[12:13], v46, s[64:65]
	ds_write_b16 v10, v12 offset:164
	v_lshrrev_b64 v[12:13], v46, s[66:67]
	ds_write_b16 v10, v12 offset:166
	s_or_b64 exec, exec, s[42:43]
	v_cmp_ge_u32_e64 s[0:1], v136, v8
	v_cmp_ge_u32_e64 s[2:3], v146, v8
	v_cmp_ge_u32_e64 s[64:65], v134, v8
	v_cmp_ge_u32_e64 s[66:67], v143, v8
	s_and_saveexec_b64 s[42:43], s[14:15]
	v_lshrrev_b64 v[12:13], v46, s[0:1]
	ds_write_b16 v10, v12 offset:168
	v_lshrrev_b64 v[12:13], v46, s[2:3]
	ds_write_b16 v10, v12 offset:170
	v_lshrrev_b64 v[12:13], v46, s[64:65]
	ds_write_b16 v10, v12 offset:172
	v_lshrrev_b64 v[12:13], v46, s[66:67]
	ds_write_b16 v10, v12 offset:174
	s_or_b64 exec, exec, s[42:43]
	s_cmp_eq_u64 s[12:13], 0
	s_cbranch_scc1 .Lmy_emit_own
	v_cmp_ge_u32_e64 s[0:1], v132, v8
	v_cmp_ge_u32_e64 s[2:3], v141, v8
	v_cmp_ge_u32_e64 s[64:65], v73, v8
	v_cmp_ge_u32_e64 s[66:67], v139, v8
	s_and_saveexec_b64 s[42:43], s[14:15]
	v_lshrrev_b64 v[12:13], v46, s[0:1]
	ds_write_b16 v10, v12 offset:176
	v_lshrrev_b64 v[12:13], v46, s[2:3]
	ds_write_b16 v10, v12 offset:178
	v_lshrrev_b64 v[12:13], v46, s[64:65]
	ds_write_b16 v10, v12 offset:180
	v_lshrrev_b64 v[12:13], v46, s[66:67]
	ds_write_b16 v10, v12 offset:182
	s_or_b64 exec, exec, s[42:43]
	v_cmp_ge_u32_e64 s[0:1], v47, v8
	v_cmp_ge_u32_e64 s[2:3], v137, v8
	v_cmp_ge_u32_e64 s[64:65], v42, v8
	v_cmp_ge_u32_e64 s[66:67], v135, v8
	s_and_saveexec_b64 s[42:43], s[14:15]
	v_lshrrev_b64 v[12:13], v46, s[0:1]
	ds_write_b16 v10, v12 offset:184
	v_lshrrev_b64 v[12:13], v46, s[2:3]
	ds_write_b16 v10, v12 offset:186
	v_lshrrev_b64 v[12:13], v46, s[64:65]
	ds_write_b16 v10, v12 offset:188
	v_lshrrev_b64 v[12:13], v46, s[66:67]
	ds_write_b16 v10, v12 offset:190
	s_or_b64 exec, exec, s[42:43]
	s_cmp_eq_u64 s[36:37], 0
	s_cbranch_scc1 .Lmy_emit_own
	v_cmp_ge_u32_e64 s[0:1], v40, v8
	v_cmp_ge_u32_e64 s[2:3], v133, v8
	v_cmp_ge_u32_e64 s[64:65], v38, v8
	v_cmp_ge_u32_e64 s[66:67], v75, v8
	s_and_saveexec_b64 s[42:43], s[14:15]
	v_lshrrev_b64 v[12:13], v46, s[0:1]
	ds_write_b16 v10, v12 offset:192
	v_lshrrev_b64 v[12:13], v46, s[2:3]
	ds_write_b16 v10, v12 offset:194
	v_lshrrev_b64 v[12:13], v46, s[64:65]
	ds_write_b16 v10, v12 offset:196
	v_lshrrev_b64 v[12:13], v46, s[66:67]
	ds_write_b16 v10, v12 offset:198
	s_or_b64 exec, exec, s[42:43]
	v_cmp_ge_u32_e64 s[0:1], v34, v8
	v_cmp_ge_u32_e64 s[2:3], v67, v8
	v_cmp_ge_u32_e64 s[64:65], v32, v8
	v_cmp_ge_u32_e64 s[66:67], v43, v8
	s_and_saveexec_b64 s[42:43], s[14:15]
	v_lshrrev_b64 v[12:13], v46, s[0:1]
	ds_write_b16 v10, v12 offset:200
	v_lshrrev_b64 v[12:13], v46, s[2:3]
	ds_write_b16 v10, v12 offset:202
	v_lshrrev_b64 v[12:13], v46, s[64:65]
	ds_write_b16 v10, v12 offset:204
	v_lshrrev_b64 v[12:13], v46, s[66:67]
	ds_write_b16 v10, v12 offset:206
	s_or_b64 exec, exec, s[42:43]
	s_cmp_eq_u64 s[38:39], 0
	s_cbranch_scc1 .Lmy_emit_own
	v_cmp_ge_u32_e64 s[0:1], v30, v8
	v_cmp_ge_u32_e64 s[2:3], v41, v8
	v_cmp_ge_u32_e64 s[64:65], v26, v8
	v_cmp_ge_u32_e64 s[66:67], v39, v8
	s_and_saveexec_b64 s[42:43], s[14:15]
	v_lshrrev_b64 v[12:13], v46, s[0:1]
	ds_write_b16 v10, v12 offset:208
	v_lshrrev_b64 v[12:13], v46, s[2:3]
	ds_write_b16 v10, v12 offset:210
	v_lshrrev_b64 v[12:13], v46, s[64:65]
	ds_write_b16 v10, v12 offset:212
	v_lshrrev_b64 v[12:13], v46, s[66:67]
	ds_write_b16 v10, v12 offset:214
	s_or_b64 exec, exec, s[42:43]
	v_cmp_ge_u32_e64 s[0:1], v24, v8
	v_cmp_ge_u32_e64 s[2:3], v35, v8
	v_cmp_ge_u32_e64 s[64:65], v22, v8
	v_cmp_ge_u32_e64 s[66:67], v33, v8
	s_and_saveexec_b64 s[42:43], s[14:15]
	v_lshrrev_b64 v[12:13], v46, s[0:1]
	ds_write_b16 v10, v12 offset:216
	v_lshrrev_b64 v[12:13], v46, s[2:3]
	ds_write_b16 v10, v12 offset:218
	v_lshrrev_b64 v[12:13], v46, s[64:65]
	ds_write_b16 v10, v12 offset:220
	v_lshrrev_b64 v[12:13], v46, s[66:67]
	ds_write_b16 v10, v12 offset:222
	s_or_b64 exec, exec, s[42:43]
	s_cmp_eq_u64 s[40:41], 0
	s_cbranch_scc1 .Lmy_emit_own
	v_cmp_ge_u32_e64 s[0:1], v19, v8
	v_cmp_ge_u32_e64 s[2:3], v31, v8
	v_cmp_ge_u32_e64 s[64:65], v18, v8
	v_cmp_ge_u32_e64 s[66:67], v27, v8
	s_and_saveexec_b64 s[42:43], s[14:15]
	v_lshrrev_b64 v[12:13], v46, s[0:1]
	ds_write_b16 v10, v12 offset:224
	v_lshrrev_b64 v[12:13], v46, s[2:3]
	ds_write_b16 v10, v12 offset:226
	v_lshrrev_b64 v[12:13], v46, s[64:65]
	ds_write_b16 v10, v12 offset:228
	v_lshrrev_b64 v[12:13], v46, s[66:67]
	ds_write_b16 v10, v12 offset:230
	s_or_b64 exec, exec, s[42:43]
	v_cmp_ge_u32_e64 s[0:1], v17, v8
	v_cmp_ge_u32_e64 s[2:3], v25, v8
	v_cmp_ge_u32_e64 s[64:65], v16, v8
	v_cmp_ge_u32_e64 s[66:67], v23, v8
	s_and_saveexec_b64 s[42:43], s[14:15]
	v_lshrrev_b64 v[12:13], v46, s[0:1]
	ds_write_b16 v10, v12 offset:232
	v_lshrrev_b64 v[12:13], v46, s[2:3]
	ds_write_b16 v10, v12 offset:234
	v_lshrrev_b64 v[12:13], v46, s[64:65]
	ds_write_b16 v10, v12 offset:236
	v_lshrrev_b64 v[12:13], v46, s[66:67]
	ds_write_b16 v10, v12 offset:238
	s_or_b64 exec, exec, s[42:43]
.Lmy_emit_own:
	v_add_u32_e32 v10, v10, v131
	v_cmp_ge_u32_e64 s[0:1], v37, v8
	v_cmp_ge_u32_e64 s[2:3], v36, v8
	v_cmp_ge_u32_e64 s[64:65], v29, v8
	v_cmp_ge_u32_e64 s[66:67], v28, v8
	s_and_saveexec_b64 s[42:43], s[14:15]
	v_lshrrev_b64 v[12:13], v46, s[0:1]
	ds_write_b16 v10, v12
	v_lshrrev_b64 v[12:13], v46, s[2:3]
	ds_write_b16 v10, v12 offset:2
	v_lshrrev_b64 v[12:13], v46, s[64:65]
	ds_write_b16 v10, v12 offset:4
	v_lshrrev_b64 v[12:13], v46, s[66:67]
	ds_write_b16 v10, v12 offset:6
	s_or_b64 exec, exec, s[42:43]
	v_cmp_ge_u32_e64 s[0:1], v21, v8
	v_cmp_ge_u32_e64 s[2:3], v20, v8
	v_cmp_ge_u32_e64 s[64:65], v15, v8
	v_cmp_ge_u32_e64 s[66:67], v14, v8
	s_and_saveexec_b64 s[42:43], s[14:15]
	v_lshrrev_b64 v[12:13], v46, s[0:1]
	ds_write_b16 v10, v12 offset:8
	v_lshrrev_b64 v[12:13], v46, s[2:3]
	ds_write_b16 v10, v12 offset:10
	v_lshrrev_b64 v[12:13], v46, s[64:65]
	ds_write_b16 v10, v12 offset:12
	v_lshrrev_b64 v[12:13], v46, s[66:67]
	ds_write_b16 v10, v12 offset:14
	s_or_b64 exec, exec, s[42:43]
	s_branch .Lmy_emit_done
.Lmy_emit_slow:
	s_and_saveexec_b64 s[42:43], s[16:17]
	s_cbranch_execz .LBB0_1265
	v_cmp_ge_u32_e64 s[64:65], v247, v8
	v_mov_b32_e32 v11, 0
	s_and_saveexec_b64 s[66:67], s[62:63]
	s_cbranch_execz .LBB0_876
	v_cmp_eq_u32_e32 vcc, v247, v8
	v_cmp_gt_u32_e64 s[0:1], v247, v8
	s_nop 0
	v_lshrrev_b64 v[12:13], v46, vcc
	v_and_b32_e32 v11, 0xffff, v12
	v_and_b32_e32 v12, v12, v88
	v_bcnt_u32_b32 v12, v12, 0
	v_cmp_lt_i32_e64 s[2:3], v12, v9
	s_and_b64 s[2:3], vcc, s[2:3]
	s_or_b64 s[0:1], s[0:1], s[2:3]
	s_andn2_b64 s[2:3], s[64:65], exec
	s_and_b64 s[0:1], s[0:1], exec
	v_bcnt_u32_b32 v11, v11, 0
	s_or_b64 s[64:65], s[2:3], s[0:1]
